# baseline (speedup 1.0000x reference)
_Z12score_kernelPKfP15HIP_vector_typeIjLj2EES0_S0_:
	s_load_dwordx4 s[4:7], s[0:1], 0x0
	s_load_dwordx4 s[32:35], s[0:1], 0x10
	s_and_b32 s15, s2, 7
	s_lshl_b32 s15, s15, 2
	s_lshr_b32 s17, s2, 6
	s_add_u32 s15, s15, s17
	s_bfe_u32 s16, s2, 0x30003
	s_mul_i32 s17, s16, 0x271
	v_add_u32_e32 v2, s17, v0
	v_lshlrev_b32_e32 v1, 2, v2
	s_movk_i32 s17, 0x271
	v_cmp_gt_u32_e32 vcc, s17, v0
	v_readfirstlane_b32 s21, v0
	s_and_b64 exec, exec, vcc
	s_mov_b64 s[18:19], exec
	s_lshr_b32 s21, s21, 6
	s_movk_i32 s13, 0x4e20
	s_mov_b32 s14, 0x3fb8aa3b
	s_mov_b32 s12, 0
	s_mov_b32 s10, 0x13d620
	s_mov_b32 s11, 0x20000
	s_mul_i32 s17, s15, 0x13d620
	s_mul_hi_u32 s20, s15, 0x13d620
	s_mov_b32 s40, 0
	s_add_u32 s41, s40, s13
	s_add_u32 s42, s41, s13
	s_add_u32 s43, s42, s13
	s_add_u32 s44, s43, s13
	s_add_u32 s45, s44, s13
	s_add_u32 s46, s45, s13
	s_add_u32 s47, s46, s13
	s_add_u32 s48, s47, s13
	s_add_u32 s49, s48, s13
	s_add_u32 s50, s49, s13
	s_add_u32 s51, s50, s13
	s_add_u32 s52, s51, s13
	s_add_u32 s53, s52, s13
	s_add_u32 s54, s53, s13
	s_add_u32 s55, s54, s13
	s_waitcnt lgkmcnt(0)
	s_add_u32 s8, s4, s17
	s_addc_u32 s9, s5, s20
	s_and_b32 s9, s9, 0xffff
	buffer_load_dword v8, v1, s[8:11], s40 offen nt
	buffer_load_dword v9, v1, s[8:11], s41 offen nt
	buffer_load_dword v10, v1, s[8:11], s42 offen nt
	buffer_load_dword v11, v1, s[8:11], s43 offen nt
	buffer_load_dword v12, v1, s[8:11], s44 offen nt
	buffer_load_dword v13, v1, s[8:11], s45 offen nt
	buffer_load_dword v14, v1, s[8:11], s46 offen nt
	buffer_load_dword v15, v1, s[8:11], s47 offen nt
	buffer_load_dword v16, v1, s[8:11], s48 offen nt
	buffer_load_dword v17, v1, s[8:11], s49 offen nt
	buffer_load_dword v18, v1, s[8:11], s50 offen nt
	buffer_load_dword v19, v1, s[8:11], s51 offen nt
	buffer_load_dword v20, v1, s[8:11], s52 offen nt
	buffer_load_dword v21, v1, s[8:11], s53 offen nt
	buffer_load_dword v22, v1, s[8:11], s54 offen nt
	buffer_load_dword v23, v1, s[8:11], s55 offen nt
	s_add_u32 s8, s8, 0x4e200
	s_addc_u32 s9, s9, 0
	buffer_load_dword v24, v1, s[8:11], s40 offen nt
	buffer_load_dword v25, v1, s[8:11], s41 offen nt
	buffer_load_dword v26, v1, s[8:11], s42 offen nt
	buffer_load_dword v27, v1, s[8:11], s43 offen nt
	buffer_load_dword v28, v1, s[8:11], s44 offen nt
	buffer_load_dword v29, v1, s[8:11], s45 offen nt
	buffer_load_dword v30, v1, s[8:11], s46 offen nt
	buffer_load_dword v31, v1, s[8:11], s47 offen nt
	buffer_load_dword v32, v1, s[8:11], s48 offen nt
	buffer_load_dword v33, v1, s[8:11], s49 offen nt
	buffer_load_dword v34, v1, s[8:11], s50 offen nt
	buffer_load_dword v35, v1, s[8:11], s51 offen nt
	buffer_load_dword v36, v1, s[8:11], s52 offen nt
	buffer_load_dword v37, v1, s[8:11], s53 offen nt
	buffer_load_dword v38, v1, s[8:11], s54 offen nt
	buffer_load_dword v39, v1, s[8:11], s55 offen nt
	s_add_u32 s8, s8, 0x4e200
	s_addc_u32 s9, s9, 0
	buffer_load_dword v40, v1, s[8:11], s40 offen nt
	buffer_load_dword v41, v1, s[8:11], s41 offen nt
	buffer_load_dword v42, v1, s[8:11], s42 offen nt
	buffer_load_dword v43, v1, s[8:11], s43 offen nt
	buffer_load_dword v44, v1, s[8:11], s44 offen nt
	buffer_load_dword v45, v1, s[8:11], s45 offen nt
	buffer_load_dword v46, v1, s[8:11], s46 offen nt
	buffer_load_dword v47, v1, s[8:11], s47 offen nt
	buffer_load_dword v48, v1, s[8:11], s48 offen nt
	buffer_load_dword v49, v1, s[8:11], s49 offen nt
	buffer_load_dword v50, v1, s[8:11], s50 offen nt
	buffer_load_dword v51, v1, s[8:11], s51 offen nt
	buffer_load_dword v52, v1, s[8:11], s52 offen nt
	buffer_load_dword v53, v1, s[8:11], s53 offen nt
	buffer_load_dword v54, v1, s[8:11], s54 offen nt
	buffer_load_dword v55, v1, s[8:11], s55 offen nt
	s_add_u32 s8, s8, 0x4e200
	s_addc_u32 s9, s9, 0
	buffer_load_dword v56, v1, s[8:11], s40 offen nt
	buffer_load_dword v57, v1, s[8:11], s41 offen nt
	buffer_load_dword v58, v1, s[8:11], s42 offen nt
	buffer_load_dword v59, v1, s[8:11], s43 offen nt
	buffer_load_dword v60, v1, s[8:11], s44 offen nt
	buffer_load_dword v61, v1, s[8:11], s45 offen nt
	buffer_load_dword v62, v1, s[8:11], s46 offen nt
	buffer_load_dword v63, v1, s[8:11], s47 offen nt
	buffer_load_dword v64, v1, s[8:11], s48 offen nt
	buffer_load_dword v65, v1, s[8:11], s49 offen nt
	buffer_load_dword v66, v1, s[8:11], s50 offen nt
	v_mul_u32_u24_e32 v3, 0x147b, v2
	v_lshrrev_b32_e32 v3, 19, v3
	v_mul_u32_u24_e32 v98, 0x64, v3
	v_sub_u32_e32 v98, v2, v98
	v_add_u32_e32 v3, -1, v3
	v_add_u32_e32 v98, -1, v98
	s_movk_i32 s17, 0x62
	v_cmp_gt_u32_e64 s[36:37], 48, v3
	v_cmp_gt_u32_e64 s[38:39], s17, v98
	s_mul_i32 s17, s15, 0x1388
	v_add_lshl_u32 v98, v2, s17, 3
	s_and_b64 s[36:37], s[36:37], s[38:39]
	s_waitcnt vmcnt(55)
	buffer_load_dword v67, v1, s[8:11], s51 offen nt
	buffer_load_dword v68, v1, s[8:11], s52 offen nt
	buffer_load_dword v69, v1, s[8:11], s53 offen nt
	buffer_load_dword v70, v1, s[8:11], s54 offen nt
	buffer_load_dword v71, v1, s[8:11], s55 offen nt
	s_add_u32 s8, s8, 0x4e200
	s_addc_u32 s9, s9, 0
	buffer_load_dword v72, v1, s[8:11], s40 offen nt
	s_waitcnt vmcnt(49)
	v_max3_f32 v76, v8, v9, v10
	v_max3_f32 v76, v76, v11, v12
	v_max3_f32 v76, v76, v13, v14
	v_max3_f32 v76, v76, v15, v16
	v_max3_f32 v76, v76, v17, v18
	v_max3_f32 v76, v76, v19, v20
	v_max3_f32 v76, v76, v21, v22
	v_max_f32_e32 v76, v76, v23
	v_pk_add_f32 v[8:9], v[8:9], v[76:77] op_sel_hi:[1,0] neg_lo:[0,1] neg_hi:[0,1]
	v_pk_add_f32 v[10:11], v[10:11], v[76:77] op_sel_hi:[1,0] neg_lo:[0,1] neg_hi:[0,1]
	v_pk_add_f32 v[12:13], v[12:13], v[76:77] op_sel_hi:[1,0] neg_lo:[0,1] neg_hi:[0,1]
	v_pk_add_f32 v[14:15], v[14:15], v[76:77] op_sel_hi:[1,0] neg_lo:[0,1] neg_hi:[0,1]
	v_pk_add_f32 v[16:17], v[16:17], v[76:77] op_sel_hi:[1,0] neg_lo:[0,1] neg_hi:[0,1]
	v_pk_add_f32 v[18:19], v[18:19], v[76:77] op_sel_hi:[1,0] neg_lo:[0,1] neg_hi:[0,1]
	v_pk_add_f32 v[20:21], v[20:21], v[76:77] op_sel_hi:[1,0] neg_lo:[0,1] neg_hi:[0,1]
	v_pk_add_f32 v[22:23], v[22:23], v[76:77] op_sel_hi:[1,0] neg_lo:[0,1] neg_hi:[0,1]
	v_or_b32_e32 v81, 0, v8
	v_or_b32_e32 v82, 1, v9
	v_min_u32_e32 v80, v81, v82
	v_or_b32_e32 v81, 2, v10
	v_or_b32_e32 v82, 3, v11
	v_min3_u32 v80, v80, v81, v82
	v_or_b32_e32 v81, 4, v12
	v_or_b32_e32 v82, 5, v13
	v_min3_u32 v80, v80, v81, v82
	v_or_b32_e32 v81, 6, v14
	v_or_b32_e32 v82, 7, v15
	v_min3_u32 v80, v80, v81, v82
	v_or_b32_e32 v81, 8, v16
	v_or_b32_e32 v82, 9, v17
	v_min3_u32 v80, v80, v81, v82
	v_or_b32_e32 v81, 10, v18
	v_or_b32_e32 v82, 11, v19
	v_min3_u32 v80, v80, v81, v82
	v_or_b32_e32 v81, 12, v20
	v_or_b32_e32 v82, 13, v21
	v_min3_u32 v80, v80, v81, v82
	v_or_b32_e32 v81, 14, v22
	v_or_b32_e32 v82, 15, v23
	v_min3_u32 v80, v80, v81, v82
	v_pk_mul_f32 v[8:9], v[8:9], s[14:15] op_sel_hi:[1,0]
	v_pk_mul_f32 v[10:11], v[10:11], s[14:15] op_sel_hi:[1,0]
	v_pk_mul_f32 v[12:13], v[12:13], s[14:15] op_sel_hi:[1,0]
	v_pk_mul_f32 v[14:15], v[14:15], s[14:15] op_sel_hi:[1,0]
	v_pk_mul_f32 v[16:17], v[16:17], s[14:15] op_sel_hi:[1,0]
	v_pk_mul_f32 v[18:19], v[18:19], s[14:15] op_sel_hi:[1,0]
	v_pk_mul_f32 v[20:21], v[20:21], s[14:15] op_sel_hi:[1,0]
	v_pk_mul_f32 v[22:23], v[22:23], s[14:15] op_sel_hi:[1,0]
	v_exp_f32_e32 v8, v8
	v_exp_f32_e32 v9, v9
	v_exp_f32_e32 v10, v10
	v_exp_f32_e32 v11, v11
	v_exp_f32_e32 v12, v12
	v_exp_f32_e32 v13, v13
	v_exp_f32_e32 v14, v14
	v_exp_f32_e32 v15, v15
	v_exp_f32_e32 v16, v16
	v_exp_f32_e32 v17, v17
	v_exp_f32_e32 v18, v18
	v_exp_f32_e32 v19, v19
	v_exp_f32_e32 v20, v20
	v_exp_f32_e32 v21, v21
	v_exp_f32_e32 v22, v22
	v_exp_f32_e32 v23, v23
	v_pk_add_f32 v[78:79], v[8:9], v[10:11]
	v_pk_add_f32 v[78:79], v[78:79], v[12:13]
	v_pk_add_f32 v[78:79], v[78:79], v[14:15]
	v_pk_add_f32 v[78:79], v[78:79], v[16:17]
	v_pk_add_f32 v[78:79], v[78:79], v[18:19]
	v_pk_add_f32 v[78:79], v[78:79], v[20:21]
	v_pk_add_f32 v[78:79], v[78:79], v[22:23]
	v_add_f32_e32 v78, v78, v79
	v_cvt_f64_f32_e32 v[86:87], v78
	v_mov_b32_e32 v75, v80
	v_mov_b32_e32 v73, v76
	s_cmp_lg_u32 s21, 0
	s_cbranch_scc1 .Lk1_nowarm0
	s_getpc_b64 s[30:31]
	v_lshlrev_b32_e32 v3, 6, v0
	global_load_dword v92, v3, s[30:31]
	s_add_u32 s30, s30, 0x1000
	s_addc_u32 s31, s31, 0
	global_load_dword v93, v3, s[30:31]
	s_add_u32 s30, s30, 0x1000
	s_addc_u32 s31, s31, 0
	global_load_dword v94, v3, s[30:31]
	s_and_b32 s30, s0, 0xfffff000
	s_mov_b32 s31, s1
	global_load_dword v95, v3, s[30:31]

.Lk1_nowarm9:
	s_waitcnt vmcnt(33)
	v_max3_f32 v76, v24, v25, v26
	v_max3_f32 v76, v76, v27, v28
	v_max3_f32 v76, v76, v29, v30
	v_max3_f32 v76, v76, v31, v32
	v_max3_f32 v76, v76, v33, v34
	v_max3_f32 v76, v76, v35, v36
	v_max3_f32 v76, v76, v37, v38
	v_max_f32_e32 v76, v76, v39
	v_max_f32_e32 v100, v73, v76
	v_cmp_gt_f32_e64 s[26:27], v76, v73
	v_sub_f32_e32 v83, v73, v100
	v_mul_f32_e32 v83, s14, v83
	v_exp_f32_e32 v83, v83
	v_pk_add_f32 v[24:25], v[24:25], v[100:101] op_sel_hi:[1,0] neg_lo:[0,1] neg_hi:[0,1]
	v_pk_add_f32 v[26:27], v[26:27], v[100:101] op_sel_hi:[1,0] neg_lo:[0,1] neg_hi:[0,1]
	v_pk_add_f32 v[28:29], v[28:29], v[100:101] op_sel_hi:[1,0] neg_lo:[0,1] neg_hi:[0,1]
	v_pk_add_f32 v[30:31], v[30:31], v[100:101] op_sel_hi:[1,0] neg_lo:[0,1] neg_hi:[0,1]
	v_pk_add_f32 v[32:33], v[32:33], v[100:101] op_sel_hi:[1,0] neg_lo:[0,1] neg_hi:[0,1]
	v_pk_add_f32 v[34:35], v[34:35], v[100:101] op_sel_hi:[1,0] neg_lo:[0,1] neg_hi:[0,1]
	v_pk_add_f32 v[36:37], v[36:37], v[100:101] op_sel_hi:[1,0] neg_lo:[0,1] neg_hi:[0,1]
	v_pk_add_f32 v[38:39], v[38:39], v[100:101] op_sel_hi:[1,0] neg_lo:[0,1] neg_hi:[0,1]
	v_cvt_f64_f32_e32 v[90:91], v83
	v_or_b32_e32 v81, 16, v24
	v_or_b32_e32 v82, 17, v25
	v_min_u32_e32 v80, v81, v82
	v_or_b32_e32 v81, 18, v26
	v_or_b32_e32 v82, 19, v27
	v_min3_u32 v80, v80, v81, v82
	v_or_b32_e32 v81, 20, v28
	v_or_b32_e32 v82, 21, v29
	v_min3_u32 v80, v80, v81, v82
	v_or_b32_e32 v81, 22, v30
	v_or_b32_e32 v82, 23, v31
	v_min3_u32 v80, v80, v81, v82
	v_or_b32_e32 v81, 24, v32
	v_or_b32_e32 v82, 25, v33
	v_min3_u32 v80, v80, v81, v82
	v_or_b32_e32 v81, 26, v34
	v_or_b32_e32 v82, 27, v35
	v_min3_u32 v80, v80, v81, v82
	v_or_b32_e32 v81, 28, v36
	v_or_b32_e32 v82, 29, v37
	v_min3_u32 v80, v80, v81, v82
	v_or_b32_e32 v81, 30, v38
	v_or_b32_e32 v82, 31, v39
	v_min3_u32 v80, v80, v81, v82
	v_pk_mul_f32 v[24:25], v[24:25], s[14:15] op_sel_hi:[1,0]
	v_pk_mul_f32 v[26:27], v[26:27], s[14:15] op_sel_hi:[1,0]
	v_pk_mul_f32 v[28:29], v[28:29], s[14:15] op_sel_hi:[1,0]
	v_pk_mul_f32 v[30:31], v[30:31], s[14:15] op_sel_hi:[1,0]
	v_pk_mul_f32 v[32:33], v[32:33], s[14:15] op_sel_hi:[1,0]
	v_pk_mul_f32 v[34:35], v[34:35], s[14:15] op_sel_hi:[1,0]
	v_pk_mul_f32 v[36:37], v[36:37], s[14:15] op_sel_hi:[1,0]
	v_pk_mul_f32 v[38:39], v[38:39], s[14:15] op_sel_hi:[1,0]
	v_exp_f32_e32 v24, v24
	v_exp_f32_e32 v25, v25
	v_exp_f32_e32 v26, v26
	v_exp_f32_e32 v27, v27
	v_exp_f32_e32 v28, v28
	v_exp_f32_e32 v29, v29
	v_exp_f32_e32 v30, v30
	v_exp_f32_e32 v31, v31
	v_exp_f32_e32 v32, v32
	v_exp_f32_e32 v33, v33
	v_exp_f32_e32 v34, v34
	v_exp_f32_e32 v35, v35
	v_exp_f32_e32 v36, v36
	v_exp_f32_e32 v37, v37
	v_exp_f32_e32 v38, v38
	v_exp_f32_e32 v39, v39
	v_pk_add_f32 v[78:79], v[24:25], v[26:27]
	v_pk_add_f32 v[78:79], v[78:79], v[28:29]
	v_pk_add_f32 v[78:79], v[78:79], v[30:31]
	v_pk_add_f32 v[78:79], v[78:79], v[32:33]
	v_pk_add_f32 v[78:79], v[78:79], v[34:35]
	v_pk_add_f32 v[78:79], v[78:79], v[36:37]
	v_pk_add_f32 v[78:79], v[78:79], v[38:39]
	v_add_f32_e32 v78, v78, v79
	v_cvt_f64_f32_e32 v[84:85], v78
	v_cndmask_b32_e64 v75, v75, v80, s[26:27]
	v_mov_b32_e32 v73, v100
	v_fma_f64 v[86:87], v[86:87], v[90:91], v[84:85]
	s_waitcnt vmcnt(17)
	v_max3_f32 v76, v40, v41, v42
	v_max3_f32 v76, v76, v43, v44
	v_max3_f32 v76, v76, v45, v46
	v_max3_f32 v76, v76, v47, v48
	v_max3_f32 v76, v76, v49, v50
	v_max3_f32 v76, v76, v51, v52
	v_max3_f32 v76, v76, v53, v54
	v_max_f32_e32 v76, v76, v55
	v_max_f32_e32 v100, v73, v76
	v_cmp_gt_f32_e64 s[26:27], v76, v73
	v_sub_f32_e32 v83, v73, v100
	v_mul_f32_e32 v83, s14, v83
	v_exp_f32_e32 v83, v83
	v_pk_add_f32 v[40:41], v[40:41], v[100:101] op_sel_hi:[1,0] neg_lo:[0,1] neg_hi:[0,1]
	v_pk_add_f32 v[42:43], v[42:43], v[100:101] op_sel_hi:[1,0] neg_lo:[0,1] neg_hi:[0,1]
	v_pk_add_f32 v[44:45], v[44:45], v[100:101] op_sel_hi:[1,0] neg_lo:[0,1] neg_hi:[0,1]
	v_pk_add_f32 v[46:47], v[46:47], v[100:101] op_sel_hi:[1,0] neg_lo:[0,1] neg_hi:[0,1]
	v_pk_add_f32 v[48:49], v[48:49], v[100:101] op_sel_hi:[1,0] neg_lo:[0,1] neg_hi:[0,1]
	v_pk_add_f32 v[50:51], v[50:51], v[100:101] op_sel_hi:[1,0] neg_lo:[0,1] neg_hi:[0,1]
	v_pk_add_f32 v[52:53], v[52:53], v[100:101] op_sel_hi:[1,0] neg_lo:[0,1] neg_hi:[0,1]
	v_pk_add_f32 v[54:55], v[54:55], v[100:101] op_sel_hi:[1,0] neg_lo:[0,1] neg_hi:[0,1]
	v_cvt_f64_f32_e32 v[90:91], v83
	v_or_b32_e32 v81, 32, v40
	v_or_b32_e32 v82, 33, v41
	v_min_u32_e32 v80, v81, v82
	v_or_b32_e32 v81, 34, v42
	v_or_b32_e32 v82, 35, v43
	v_min3_u32 v80, v80, v81, v82
	v_or_b32_e32 v81, 36, v44
	v_or_b32_e32 v82, 37, v45
	v_min3_u32 v80, v80, v81, v82
	v_or_b32_e32 v81, 38, v46
	v_or_b32_e32 v82, 39, v47
	v_min3_u32 v80, v80, v81, v82
	v_or_b32_e32 v81, 40, v48
	v_or_b32_e32 v82, 41, v49
	v_min3_u32 v80, v80, v81, v82
	v_or_b32_e32 v81, 42, v50
	v_or_b32_e32 v82, 43, v51
	v_min3_u32 v80, v80, v81, v82
	v_or_b32_e32 v81, 44, v52
	v_or_b32_e32 v82, 45, v53
	v_min3_u32 v80, v80, v81, v82
	v_or_b32_e32 v81, 46, v54
	v_or_b32_e32 v82, 47, v55
	v_min3_u32 v80, v80, v81, v82
	v_pk_mul_f32 v[40:41], v[40:41], s[14:15] op_sel_hi:[1,0]
	v_pk_mul_f32 v[42:43], v[42:43], s[14:15] op_sel_hi:[1,0]
	v_pk_mul_f32 v[44:45], v[44:45], s[14:15] op_sel_hi:[1,0]
	v_pk_mul_f32 v[46:47], v[46:47], s[14:15] op_sel_hi:[1,0]
	v_pk_mul_f32 v[48:49], v[48:49], s[14:15] op_sel_hi:[1,0]
	v_pk_mul_f32 v[50:51], v[50:51], s[14:15] op_sel_hi:[1,0]
	v_pk_mul_f32 v[52:53], v[52:53], s[14:15] op_sel_hi:[1,0]
	v_pk_mul_f32 v[54:55], v[54:55], s[14:15] op_sel_hi:[1,0]
	v_exp_f32_e32 v40, v40
	v_exp_f32_e32 v41, v41
	v_exp_f32_e32 v42, v42
	v_exp_f32_e32 v43, v43
	v_exp_f32_e32 v44, v44
	v_exp_f32_e32 v45, v45
	v_exp_f32_e32 v46, v46
	v_exp_f32_e32 v47, v47
	v_exp_f32_e32 v48, v48
	v_exp_f32_e32 v49, v49
	v_exp_f32_e32 v50, v50
	v_exp_f32_e32 v51, v51
	v_exp_f32_e32 v52, v52
	v_exp_f32_e32 v53, v53
	v_exp_f32_e32 v54, v54
	v_exp_f32_e32 v55, v55
	v_pk_add_f32 v[78:79], v[40:41], v[42:43]
	v_pk_add_f32 v[78:79], v[78:79], v[44:45]
	v_pk_add_f32 v[78:79], v[78:79], v[46:47]
	v_pk_add_f32 v[78:79], v[78:79], v[48:49]
	v_pk_add_f32 v[78:79], v[78:79], v[50:51]
	v_pk_add_f32 v[78:79], v[78:79], v[52:53]
	v_pk_add_f32 v[78:79], v[78:79], v[54:55]
	v_add_f32_e32 v78, v78, v79
	v_cvt_f64_f32_e32 v[84:85], v78
	v_cndmask_b32_e64 v75, v75, v80, s[26:27]
	v_mov_b32_e32 v73, v100
	v_fma_f64 v[86:87], v[86:87], v[90:91], v[84:85]
	s_waitcnt vmcnt(9)
	v_max3_f32 v76, v56, v57, v58
	v_max3_f32 v76, v76, v59, v60
	v_max3_f32 v76, v76, v61, v62
	v_max_f32_e32 v76, v76, v63
	v_max_f32_e32 v100, v73, v76
	v_cmp_gt_f32_e64 s[26:27], v76, v73
	v_sub_f32_e32 v83, v73, v100
	v_mul_f32_e32 v83, s14, v83
	v_exp_f32_e32 v83, v83
	v_pk_add_f32 v[56:57], v[56:57], v[100:101] op_sel_hi:[1,0] neg_lo:[0,1] neg_hi:[0,1]
	v_pk_add_f32 v[58:59], v[58:59], v[100:101] op_sel_hi:[1,0] neg_lo:[0,1] neg_hi:[0,1]
	v_pk_add_f32 v[60:61], v[60:61], v[100:101] op_sel_hi:[1,0] neg_lo:[0,1] neg_hi:[0,1]
	v_pk_add_f32 v[62:63], v[62:63], v[100:101] op_sel_hi:[1,0] neg_lo:[0,1] neg_hi:[0,1]
	v_cvt_f64_f32_e32 v[90:91], v83
	v_or_b32_e32 v81, 48, v56
	v_or_b32_e32 v82, 49, v57
	v_min_u32_e32 v80, v81, v82
	v_or_b32_e32 v81, 50, v58
	v_or_b32_e32 v82, 51, v59
	v_min3_u32 v80, v80, v81, v82
	v_or_b32_e32 v81, 52, v60
	v_or_b32_e32 v82, 53, v61
	v_min3_u32 v80, v80, v81, v82
	v_or_b32_e32 v81, 54, v62
	v_or_b32_e32 v82, 55, v63
	v_min3_u32 v80, v80, v81, v82
	v_pk_mul_f32 v[56:57], v[56:57], s[14:15] op_sel_hi:[1,0]
	v_pk_mul_f32 v[58:59], v[58:59], s[14:15] op_sel_hi:[1,0]
	v_pk_mul_f32 v[60:61], v[60:61], s[14:15] op_sel_hi:[1,0]
	v_pk_mul_f32 v[62:63], v[62:63], s[14:15] op_sel_hi:[1,0]
	v_exp_f32_e32 v56, v56
	v_exp_f32_e32 v57, v57
	v_exp_f32_e32 v58, v58
	v_exp_f32_e32 v59, v59
	v_exp_f32_e32 v60, v60
	v_exp_f32_e32 v61, v61
	v_exp_f32_e32 v62, v62
	v_exp_f32_e32 v63, v63
	v_pk_add_f32 v[78:79], v[56:57], v[58:59]
	v_pk_add_f32 v[78:79], v[78:79], v[60:61]
	v_pk_add_f32 v[78:79], v[78:79], v[62:63]
	v_add_f32_e32 v78, v78, v79
	v_cvt_f64_f32_e32 v[84:85], v78
	v_cndmask_b32_e64 v75, v75, v80, s[26:27]
	v_mov_b32_e32 v73, v100
	v_fma_f64 v[86:87], v[86:87], v[90:91], v[84:85]
	s_waitcnt vmcnt(5)
	v_max3_f32 v76, v64, v65, v66
	v_max_f32_e32 v76, v76, v67
	v_max_f32_e32 v100, v73, v76
	v_cmp_gt_f32_e64 s[26:27], v76, v73
	v_sub_f32_e32 v83, v73, v100
	v_mul_f32_e32 v83, s14, v83
	v_exp_f32_e32 v83, v83
	v_pk_add_f32 v[64:65], v[64:65], v[100:101] op_sel_hi:[1,0] neg_lo:[0,1] neg_hi:[0,1]
	v_pk_add_f32 v[66:67], v[66:67], v[100:101] op_sel_hi:[1,0] neg_lo:[0,1] neg_hi:[0,1]
	v_cvt_f64_f32_e32 v[90:91], v83
	v_or_b32_e32 v81, 56, v64
	v_or_b32_e32 v82, 57, v65
	v_min_u32_e32 v80, v81, v82
	v_or_b32_e32 v81, 58, v66
	v_or_b32_e32 v82, 59, v67
	v_min3_u32 v80, v80, v81, v82
	v_pk_mul_f32 v[64:65], v[64:65], s[14:15] op_sel_hi:[1,0]
	v_pk_mul_f32 v[66:67], v[66:67], s[14:15] op_sel_hi:[1,0]
	v_exp_f32_e32 v64, v64
	v_exp_f32_e32 v65, v65
	v_exp_f32_e32 v66, v66
	v_exp_f32_e32 v67, v67
	s_nop 0
	v_pk_add_f32 v[78:79], v[64:65], v[66:67]
	v_add_f32_e32 v78, v78, v79
	v_cvt_f64_f32_e32 v[84:85], v78
	v_cndmask_b32_e64 v75, v75, v80, s[26:27]
	v_mov_b32_e32 v73, v100
	v_fma_f64 v[86:87], v[86:87], v[90:91], v[84:85]
	s_waitcnt vmcnt(0)
	v_max3_f32 v76, v68, v69, v70
	v_max3_f32 v76, v76, v71, v72
	v_max_f32_e32 v100, v73, v76
	v_cmp_gt_f32_e64 s[26:27], v76, v73
	v_sub_f32_e32 v83, v73, v100
	v_mul_f32_e32 v83, s14, v83
	v_exp_f32_e32 v83, v83
	v_pk_add_f32 v[68:69], v[68:69], v[100:101] op_sel_hi:[1,0] neg_lo:[0,1] neg_hi:[0,1]
	v_pk_add_f32 v[70:71], v[70:71], v[100:101] op_sel_hi:[1,0] neg_lo:[0,1] neg_hi:[0,1]
	v_sub_f32_e32 v72, v72, v100
	v_cvt_f64_f32_e32 v[90:91], v83
	v_or_b32_e32 v81, 60, v68
	v_or_b32_e32 v82, 61, v69
	v_min_u32_e32 v80, v81, v82
	v_or_b32_e32 v81, 62, v70
	v_or_b32_e32 v82, 63, v71
	v_min3_u32 v80, v80, v81, v82
	v_or_b32_e32 v81, 64, v72
	v_min_u32_e32 v80, v80, v81
	v_pk_mul_f32 v[68:69], v[68:69], s[14:15] op_sel_hi:[1,0]
	v_pk_mul_f32 v[70:71], v[70:71], s[14:15] op_sel_hi:[1,0]
	v_mul_f32_e32 v72, s14, v72
	v_exp_f32_e32 v68, v68
	v_exp_f32_e32 v69, v69
	v_exp_f32_e32 v70, v70
	v_exp_f32_e32 v71, v71
	v_exp_f32_e32 v72, v72
	v_cndmask_b32_e64 v75, v75, v80, s[26:27]
	v_pk_add_f32 v[78:79], v[68:69], v[70:71]
	v_add_f32_e32 v78, v78, v79
	v_add_f32_e32 v78, v78, v72
	v_cvt_f64_f32_e32 v[84:85], v78
	v_fma_f64 v[86:87], v[86:87], v[90:91], v[84:85]
	v_rcp_f64_e32 v[88:89], v[86:87]
	v_cmp_gt_u32_e32 vcc, 64, v75
	s_and_b64 vcc, vcc, s[36:37]
	v_fma_f64 v[90:91], -v[86:87], v[88:89], 1.0
	v_fma_f64 v[88:89], v[90:91], v[88:89], v[88:89]
	v_cvt_f32_f64_e32 v3, v[88:89]
	v_cndmask_b32_e32 v74, 0, v3, vcc
	global_store_dwordx2 v98, v[74:75], s[6:7]
